# fp8 expert GEMMs: unscaled v_mfma_f32_16x16x128_f8f6f4 (fp8 e4m3 operands, f32 accumulate, same numerics) instead of the _scale_ form with unit scales - 8-byte encoding, no scale operand reads
# speedup vs baseline: 1.0097x; 1.0068x over previous
.LBB0_48:
	s_ashr_i32 s51, s50, 31
	s_lshl_b64 s[58:59], s[50:51], 18
	s_add_u32 s58, s14, s58
	s_addc_u32 s59, s15, s59
	s_and_b64 s[60:61], s[54:55], exec
	s_cselect_b32 s6, s59, s27
	s_cselect_b32 s51, s58, s26
	s_ashr_i32 s53, s52, 31
	s_lshl_b64 s[60:61], s[52:53], 20
	s_add_u32 s4, s16, s60
	s_addc_u32 s53, s17, s61
	s_ashr_i32 s49, s48, 31
	s_lshl_b64 s[60:61], s[48:49], 18
	s_add_u32 s60, s4, s60
	s_addc_u32 s61, s53, s61
	s_and_b64 s[68:69], s[54:55], exec
	s_cselect_b32 s49, s61, s37
	s_cselect_b32 s53, s60, s36
	s_add_u32 s26, s26, 0x20080
	s_addc_u32 s27, s27, 0
	s_add_u32 s65, s36, 0x100
	s_addc_u32 s74, s37, 0
	s_mov_b32 s92, -2
	s_add_u32 s36, s26, 0xfffe0080
	s_addc_u32 s37, s27, -1
	s_add_i32 s4, 0, 0x10000
	s_cmp_eq_u32 s92, 4
	s_cselect_b32 s69, s6, s37
	s_cselect_b32 s68, s51, s36
	s_cselect_b32 s37, s49, s74
	s_cselect_b32 s36, s53, s65
	s_add_i32 s93, 0, 0x14000
	v_add_u32_e32 v2, s4, v184
	v_add_u32_e32 v14, s93, v184
	ds_read_b128 v[18:21], v2
	ds_read_b128 v[22:25], v2 offset:1024
	ds_read_b128 v[26:29], v2 offset:2048
	ds_read_b128 v[30:33], v2 offset:3072
	ds_read_b128 v[2:5], v14
	ds_read_b128 v[6:9], v14 offset:1024
	ds_read_b128 v[10:13], v14 offset:2048
	ds_read_b128 v[14:17], v14 offset:3072
	v_lshl_add_u64 v[188:189], s[26:27], 0, v[170:171]
	s_add_i32 m0, s63, 0xc000
	ds_read_b128 v[174:177], v187
	ds_read_b128 v[178:181], v187 offset:1024
	ds_read_b128 v[196:199], v187 offset:2048
	ds_read_b128 v[200:203], v187 offset:3072
	ds_read_b128 v[204:207], v187 offset:4096
	ds_read_b128 v[208:211], v187 offset:5120
	ds_read_b128 v[212:215], v187 offset:6144
	ds_read_b128 v[216:219], v187 offset:7168
	global_load_lds_dwordx4 v[188:189], off
	v_lshl_add_u64 v[188:189], s[26:27], 0, v[172:173]
	s_add_i32 m0, s63, 0xe000
	s_nop 0
	global_load_lds_dwordx4 v[188:189], off
	s_waitcnt vmcnt(8)
	s_waitcnt lgkmcnt(0)
	s_barrier
	s_setprio 1
	s_waitcnt lgkmcnt(0)
	v_mfma_f32_16x16x128_f8f6f4 v[158:161], v[18:25], v[174:181], 0
	v_mfma_f32_16x16x128_f8f6f4 v[154:157], v[26:33], v[174:181], 0
	v_mfma_f32_16x16x128_f8f6f4 v[150:153], v[18:25], v[196:203], 0
	v_mfma_f32_16x16x128_f8f6f4 v[146:149], v[26:33], v[196:203], 0
	v_mfma_f32_16x16x128_f8f6f4 v[126:129], v[18:25], v[204:211], 0
	v_mfma_f32_16x16x128_f8f6f4 v[122:125], v[26:33], v[204:211], 0
	v_mfma_f32_16x16x128_f8f6f4 v[118:121], v[18:25], v[212:219], 0
	v_mfma_f32_16x16x128_f8f6f4 v[114:117], v[26:33], v[212:219], 0
	s_setprio 0
	s_setprio 1
	v_mfma_f32_16x16x128_f8f6f4 v[142:145], v[2:9], v[174:181], 0
	v_mfma_f32_16x16x128_f8f6f4 v[138:141], v[10:17], v[174:181], 0
	v_mfma_f32_16x16x128_f8f6f4 v[134:137], v[2:9], v[196:203], 0
	v_mfma_f32_16x16x128_f8f6f4 v[130:133], v[10:17], v[196:203], 0
	v_mfma_f32_16x16x128_f8f6f4 v[110:113], v[2:9], v[204:211], 0
	v_mfma_f32_16x16x128_f8f6f4 v[106:109], v[10:17], v[204:211], 0
	v_mfma_f32_16x16x128_f8f6f4 v[102:105], v[2:9], v[212:219], 0
	v_mfma_f32_16x16x128_f8f6f4 v[98:101], v[10:17], v[212:219], 0
	s_setprio 0
	s_barrier
	s_add_i32 s4, s4, s45
	v_lshl_add_u64 v[174:175], s[36:37], 0, v[0:1]
	s_mov_b32 m0, s4
	ds_read_b128 v[196:199], v187 offset:16384
	ds_read_b128 v[200:203], v187 offset:17408
	ds_read_b128 v[204:207], v187 offset:18432
	ds_read_b128 v[208:211], v187 offset:19456
	ds_read_b128 v[212:215], v187 offset:20480
	ds_read_b128 v[216:219], v187 offset:21504
	ds_read_b128 v[234:237], v187 offset:22528
	ds_read_b128 v[238:241], v187 offset:23552
	global_load_lds_dwordx4 v[174:175], off
	s_add_i32 m0, s4, 0x2000
	s_add_u32 s86, s36, 0x20000
	v_lshl_add_u64 v[176:177], s[36:37], 0, v[166:167]
	s_addc_u32 s87, s37, 0
	s_add_i32 s4, s93, s45
	global_load_lds_dwordx4 v[176:177], off
	v_lshl_add_u64 v[178:179], s[86:87], 0, v[0:1]
	s_mov_b32 m0, s4
	v_lshl_add_u64 v[180:181], s[68:69], 0, v[164:165]
	global_load_lds_dwordx4 v[178:179], off
	v_lshl_add_u64 v[178:179], s[86:87], 0, v[166:167]
	s_add_i32 m0, s4, 0x2000
	s_nop 0
	global_load_lds_dwordx4 v[178:179], off
	v_lshl_add_u64 v[178:179], s[68:69], 0, v[162:163]
	s_mov_b32 m0, s63
	s_nop 0
	global_load_lds_dwordx4 v[178:179], off
	s_mov_b32 m0, s67
	s_nop 0
	global_load_lds_dwordx4 v[180:181], off
	s_waitcnt vmcnt(8)
	s_waitcnt lgkmcnt(0)
	s_barrier
	s_setprio 1
	s_waitcnt lgkmcnt(0)
	v_mfma_f32_16x16x128_f8f6f4 v[94:97], v[18:25], v[196:203], 0
	v_mfma_f32_16x16x128_f8f6f4 v[90:93], v[26:33], v[196:203], 0
	v_mfma_f32_16x16x128_f8f6f4 v[86:89], v[18:25], v[204:211], 0
	v_mfma_f32_16x16x128_f8f6f4 v[82:85], v[26:33], v[204:211], 0
	v_mfma_f32_16x16x128_f8f6f4 v[62:65], v[18:25], v[212:219], 0
	v_mfma_f32_16x16x128_f8f6f4 v[58:61], v[26:33], v[212:219], 0
	v_mfma_f32_16x16x128_f8f6f4 v[54:57], v[18:25], v[234:241], 0
	v_mfma_f32_16x16x128_f8f6f4 v[50:53], v[26:33], v[234:241], 0
	s_setprio 0
	s_setprio 1
	v_mfma_f32_16x16x128_f8f6f4 v[78:81], v[2:9], v[196:203], 0
	v_mfma_f32_16x16x128_f8f6f4 v[74:77], v[10:17], v[196:203], 0
	v_mfma_f32_16x16x128_f8f6f4 v[70:73], v[2:9], v[204:211], 0
	v_mfma_f32_16x16x128_f8f6f4 v[66:69], v[10:17], v[204:211], 0
	v_mfma_f32_16x16x128_f8f6f4 v[46:49], v[2:9], v[212:219], 0
	v_mfma_f32_16x16x128_f8f6f4 v[42:45], v[10:17], v[212:219], 0
	v_mfma_f32_16x16x128_f8f6f4 v[38:41], v[2:9], v[234:241], 0
	v_mfma_f32_16x16x128_f8f6f4 v[34:37], v[10:17], v[234:241], 0
	s_setprio 0
	s_barrier
	s_add_i32 s4, 0, 0x18000
	s_add_i32 s86, 0, 0x1c000
	v_add_u32_e32 v14, s4, v184
	v_add_u32_e32 v30, s86, v184
	ds_read_b128 v[2:5], v14
	ds_read_b128 v[6:9], v14 offset:1024
	ds_read_b128 v[10:13], v14 offset:2048
	ds_read_b128 v[14:17], v14 offset:3072
	ds_read_b128 v[18:21], v30
	ds_read_b128 v[22:25], v30 offset:1024
	ds_read_b128 v[26:29], v30 offset:2048
	ds_read_b128 v[30:33], v30 offset:3072
	s_add_u32 s68, s68, 0x20000
	s_addc_u32 s69, s69, 0
	s_mov_b32 m0, s73
	v_lshl_add_u64 v[188:189], s[68:69], 0, v[162:163]
	ds_read_b128 v[196:199], v187 offset:32768
	ds_read_b128 v[200:203], v187 offset:33792
	ds_read_b128 v[204:207], v187 offset:34816
	ds_read_b128 v[208:211], v187 offset:35840
	ds_read_b128 v[212:215], v187 offset:36864
	ds_read_b128 v[216:219], v187 offset:37888
	ds_read_b128 v[234:237], v187 offset:38912
	ds_read_b128 v[238:241], v187 offset:39936
	global_load_lds_dwordx4 v[188:189], off
	v_lshl_add_u64 v[188:189], s[68:69], 0, v[164:165]
	s_mov_b32 m0, s75
	s_nop 0
	global_load_lds_dwordx4 v[188:189], off
	s_waitcnt vmcnt(8)
	s_waitcnt lgkmcnt(0)
	s_barrier
	s_setprio 1
	s_waitcnt lgkmcnt(0)
	v_mfma_f32_16x16x128_f8f6f4 v[158:161], v[2:9], v[196:203], v[158:161]
	v_mfma_f32_16x16x128_f8f6f4 v[154:157], v[10:17], v[196:203], v[154:157]
	v_mfma_f32_16x16x128_f8f6f4 v[150:153], v[2:9], v[204:211], v[150:153]
	v_mfma_f32_16x16x128_f8f6f4 v[146:149], v[10:17], v[204:211], v[146:149]
	v_mfma_f32_16x16x128_f8f6f4 v[126:129], v[2:9], v[212:219], v[126:129]
	v_mfma_f32_16x16x128_f8f6f4 v[122:125], v[10:17], v[212:219], v[122:125]
	v_mfma_f32_16x16x128_f8f6f4 v[118:121], v[2:9], v[234:241], v[118:121]
	v_mfma_f32_16x16x128_f8f6f4 v[114:117], v[10:17], v[234:241], v[114:117]
	s_setprio 0
	s_setprio 1
	v_mfma_f32_16x16x128_f8f6f4 v[142:145], v[18:25], v[196:203], v[142:145]
	v_mfma_f32_16x16x128_f8f6f4 v[138:141], v[26:33], v[196:203], v[138:141]
	v_mfma_f32_16x16x128_f8f6f4 v[134:137], v[18:25], v[204:211], v[134:137]
	v_mfma_f32_16x16x128_f8f6f4 v[130:133], v[26:33], v[204:211], v[130:133]
	v_mfma_f32_16x16x128_f8f6f4 v[110:113], v[18:25], v[212:219], v[110:113]
	v_mfma_f32_16x16x128_f8f6f4 v[106:109], v[26:33], v[212:219], v[106:109]
	v_mfma_f32_16x16x128_f8f6f4 v[102:105], v[18:25], v[234:241], v[102:105]
	v_mfma_f32_16x16x128_f8f6f4 v[98:101], v[26:33], v[234:241], v[98:101]
	s_setprio 0
	s_barrier
	s_add_i32 s4, s4, s45
	v_lshl_add_u64 v[174:175], v[174:175], 0, s[22:23]
	s_mov_b32 m0, s4
	ds_read_b128 v[196:199], v187 offset:49152
	ds_read_b128 v[200:203], v187 offset:50176
	ds_read_b128 v[204:207], v187 offset:51200
	ds_read_b128 v[208:211], v187 offset:52224
	ds_read_b128 v[212:215], v187 offset:53248
	ds_read_b128 v[216:219], v187 offset:54272
	ds_read_b128 v[234:237], v187 offset:55296
	ds_read_b128 v[238:241], v187 offset:56320
	global_load_lds_dwordx4 v[174:175], off
	s_add_i32 m0, s4, 0x2000
	s_add_u32 s36, s36, 0x20080
	v_lshl_add_u64 v[174:175], v[176:177], 0, s[22:23]
	s_addc_u32 s37, s37, 0
	s_add_i32 s4, s86, s45
	global_load_lds_dwordx4 v[174:175], off
	v_lshl_add_u64 v[174:175], s[36:37], 0, v[0:1]
	s_mov_b32 m0, s4
	s_nop 0
	global_load_lds_dwordx4 v[174:175], off
	v_lshl_add_u64 v[174:175], s[36:37], 0, v[166:167]
	s_add_i32 m0, s4, 0x2000
	s_nop 0
	global_load_lds_dwordx4 v[174:175], off
	v_lshl_add_u64 v[174:175], v[178:179], 0, s[22:23]
	s_mov_b32 m0, s79
	s_nop 0
	global_load_lds_dwordx4 v[174:175], off
	v_lshl_add_u64 v[174:175], v[180:181], 0, s[22:23]
	s_mov_b32 m0, s82
	s_nop 0
	global_load_lds_dwordx4 v[174:175], off
	s_waitcnt vmcnt(8)
	s_waitcnt lgkmcnt(0)
	s_barrier
	s_setprio 1
	s_waitcnt lgkmcnt(0)
	v_mfma_f32_16x16x128_f8f6f4 v[94:97], v[2:9], v[196:203], v[94:97]
	v_mfma_f32_16x16x128_f8f6f4 v[90:93], v[10:17], v[196:203], v[90:93]
	v_mfma_f32_16x16x128_f8f6f4 v[86:89], v[2:9], v[204:211], v[86:89]
	v_mfma_f32_16x16x128_f8f6f4 v[82:85], v[10:17], v[204:211], v[82:85]
	v_mfma_f32_16x16x128_f8f6f4 v[62:65], v[2:9], v[212:219], v[62:65]
	v_mfma_f32_16x16x128_f8f6f4 v[58:61], v[10:17], v[212:219], v[58:61]
	v_mfma_f32_16x16x128_f8f6f4 v[54:57], v[2:9], v[234:241], v[54:57]
	v_mfma_f32_16x16x128_f8f6f4 v[50:53], v[10:17], v[234:241], v[50:53]
	s_setprio 0
	s_setprio 1
	v_mfma_f32_16x16x128_f8f6f4 v[78:81], v[18:25], v[196:203], v[78:81]
	v_mfma_f32_16x16x128_f8f6f4 v[74:77], v[26:33], v[196:203], v[74:77]
	v_mfma_f32_16x16x128_f8f6f4 v[70:73], v[18:25], v[204:211], v[70:73]
	v_mfma_f32_16x16x128_f8f6f4 v[66:69], v[26:33], v[204:211], v[66:69]
	v_mfma_f32_16x16x128_f8f6f4 v[46:49], v[18:25], v[212:219], v[46:49]
	v_mfma_f32_16x16x128_f8f6f4 v[42:45], v[26:33], v[212:219], v[42:45]
	v_mfma_f32_16x16x128_f8f6f4 v[38:41], v[18:25], v[234:241], v[38:41]
	v_mfma_f32_16x16x128_f8f6f4 v[34:37], v[26:33], v[234:241], v[34:37]
	s_setprio 0
	s_barrier
	s_add_i32 s92, s92, 2
	s_add_u32 s26, s26, 0x100
	s_addc_u32 s27, s27, 0
	s_add_u32 s65, s65, 0x100
	s_addc_u32 s74, s74, 0
.LBB0_49:
	s_add_u32 s36, s26, 0xfffe0080
	s_addc_u32 s37, s27, -1
	s_add_i32 s4, 0, 0x10000
	s_cmp_eq_u32 s92, 4
	s_cselect_b32 s69, s6, s37
	s_cselect_b32 s68, s51, s36
	s_cselect_b32 s37, s49, s74
	s_cselect_b32 s36, s53, s65
	s_add_i32 s93, 0, 0x14000
	v_add_u32_e32 v2, s4, v184
	v_add_u32_e32 v14, s93, v184
	ds_read_b128 v[18:21], v2
	ds_read_b128 v[22:25], v2 offset:1024
	ds_read_b128 v[26:29], v2 offset:2048
	ds_read_b128 v[30:33], v2 offset:3072
	ds_read_b128 v[2:5], v14
	ds_read_b128 v[6:9], v14 offset:1024
	ds_read_b128 v[10:13], v14 offset:2048
	ds_read_b128 v[14:17], v14 offset:3072
	v_lshl_add_u64 v[188:189], s[26:27], 0, v[170:171]
	s_add_i32 m0, s63, 0xc000
	ds_read_b128 v[174:177], v187
	ds_read_b128 v[178:181], v187 offset:1024
	ds_read_b128 v[196:199], v187 offset:2048
	ds_read_b128 v[200:203], v187 offset:3072
	ds_read_b128 v[204:207], v187 offset:4096
	ds_read_b128 v[208:211], v187 offset:5120
	ds_read_b128 v[212:215], v187 offset:6144
	ds_read_b128 v[216:219], v187 offset:7168
	global_load_lds_dwordx4 v[188:189], off
	v_lshl_add_u64 v[188:189], s[26:27], 0, v[172:173]
	s_add_i32 m0, s63, 0xe000
	s_nop 0
	global_load_lds_dwordx4 v[188:189], off
	s_waitcnt vmcnt(8)
	s_waitcnt lgkmcnt(0)
	s_barrier
	s_setprio 1
	s_waitcnt lgkmcnt(0)
	v_mfma_f32_16x16x128_f8f6f4 v[158:161], v[18:25], v[174:181], v[158:161]
	v_mfma_f32_16x16x128_f8f6f4 v[154:157], v[26:33], v[174:181], v[154:157]
	v_mfma_f32_16x16x128_f8f6f4 v[150:153], v[18:25], v[196:203], v[150:153]
	v_mfma_f32_16x16x128_f8f6f4 v[146:149], v[26:33], v[196:203], v[146:149]
	v_mfma_f32_16x16x128_f8f6f4 v[126:129], v[18:25], v[204:211], v[126:129]
	v_mfma_f32_16x16x128_f8f6f4 v[122:125], v[26:33], v[204:211], v[122:125]
	v_mfma_f32_16x16x128_f8f6f4 v[118:121], v[18:25], v[212:219], v[118:121]
	v_mfma_f32_16x16x128_f8f6f4 v[114:117], v[26:33], v[212:219], v[114:117]
	s_setprio 0
	s_setprio 1
	v_mfma_f32_16x16x128_f8f6f4 v[142:145], v[2:9], v[174:181], v[142:145]
	v_mfma_f32_16x16x128_f8f6f4 v[138:141], v[10:17], v[174:181], v[138:141]
	v_mfma_f32_16x16x128_f8f6f4 v[134:137], v[2:9], v[196:203], v[134:137]
	v_mfma_f32_16x16x128_f8f6f4 v[130:133], v[10:17], v[196:203], v[130:133]
	v_mfma_f32_16x16x128_f8f6f4 v[110:113], v[2:9], v[204:211], v[110:113]
	v_mfma_f32_16x16x128_f8f6f4 v[106:109], v[10:17], v[204:211], v[106:109]
	v_mfma_f32_16x16x128_f8f6f4 v[102:105], v[2:9], v[212:219], v[102:105]
	v_mfma_f32_16x16x128_f8f6f4 v[98:101], v[10:17], v[212:219], v[98:101]
	s_setprio 0
	s_barrier
	s_add_i32 s4, s4, s45
	v_lshl_add_u64 v[174:175], s[36:37], 0, v[0:1]
	s_mov_b32 m0, s4
	ds_read_b128 v[196:199], v187 offset:16384
	ds_read_b128 v[200:203], v187 offset:17408
	ds_read_b128 v[204:207], v187 offset:18432
	ds_read_b128 v[208:211], v187 offset:19456
	ds_read_b128 v[212:215], v187 offset:20480
	ds_read_b128 v[216:219], v187 offset:21504
	ds_read_b128 v[234:237], v187 offset:22528
	ds_read_b128 v[238:241], v187 offset:23552
	global_load_lds_dwordx4 v[174:175], off
	s_add_i32 m0, s4, 0x2000
	s_add_u32 s86, s36, 0x20000
	v_lshl_add_u64 v[176:177], s[36:37], 0, v[166:167]
	s_addc_u32 s87, s37, 0
	s_add_i32 s4, s93, s45
	global_load_lds_dwordx4 v[176:177], off
	v_lshl_add_u64 v[178:179], s[86:87], 0, v[0:1]
	s_mov_b32 m0, s4
	v_lshl_add_u64 v[180:181], s[68:69], 0, v[164:165]
	global_load_lds_dwordx4 v[178:179], off
	v_lshl_add_u64 v[178:179], s[86:87], 0, v[166:167]
	s_add_i32 m0, s4, 0x2000
	s_nop 0
	global_load_lds_dwordx4 v[178:179], off
	v_lshl_add_u64 v[178:179], s[68:69], 0, v[162:163]
	s_mov_b32 m0, s63
	s_nop 0
	global_load_lds_dwordx4 v[178:179], off
	s_mov_b32 m0, s67
	s_nop 0
	global_load_lds_dwordx4 v[180:181], off
	s_waitcnt vmcnt(8)
	s_waitcnt lgkmcnt(0)
	s_barrier
	s_setprio 1
	s_waitcnt lgkmcnt(0)
	v_mfma_f32_16x16x128_f8f6f4 v[94:97], v[18:25], v[196:203], v[94:97]
	v_mfma_f32_16x16x128_f8f6f4 v[90:93], v[26:33], v[196:203], v[90:93]
	v_mfma_f32_16x16x128_f8f6f4 v[86:89], v[18:25], v[204:211], v[86:89]
	v_mfma_f32_16x16x128_f8f6f4 v[82:85], v[26:33], v[204:211], v[82:85]
	v_mfma_f32_16x16x128_f8f6f4 v[62:65], v[18:25], v[212:219], v[62:65]
	v_mfma_f32_16x16x128_f8f6f4 v[58:61], v[26:33], v[212:219], v[58:61]
	v_mfma_f32_16x16x128_f8f6f4 v[54:57], v[18:25], v[234:241], v[54:57]
	v_mfma_f32_16x16x128_f8f6f4 v[50:53], v[26:33], v[234:241], v[50:53]
	s_setprio 0
	s_setprio 1
	v_mfma_f32_16x16x128_f8f6f4 v[78:81], v[2:9], v[196:203], v[78:81]
	v_mfma_f32_16x16x128_f8f6f4 v[74:77], v[10:17], v[196:203], v[74:77]
	v_mfma_f32_16x16x128_f8f6f4 v[70:73], v[2:9], v[204:211], v[70:73]
	v_mfma_f32_16x16x128_f8f6f4 v[66:69], v[10:17], v[204:211], v[66:69]
	v_mfma_f32_16x16x128_f8f6f4 v[46:49], v[2:9], v[212:219], v[46:49]
	v_mfma_f32_16x16x128_f8f6f4 v[42:45], v[10:17], v[212:219], v[42:45]
	v_mfma_f32_16x16x128_f8f6f4 v[38:41], v[2:9], v[234:241], v[38:41]
	v_mfma_f32_16x16x128_f8f6f4 v[34:37], v[10:17], v[234:241], v[34:37]
	s_setprio 0
	s_barrier
	s_add_i32 s4, 0, 0x18000
	s_add_i32 s86, 0, 0x1c000
	v_add_u32_e32 v14, s4, v184
	v_add_u32_e32 v30, s86, v184
	ds_read_b128 v[2:5], v14
	ds_read_b128 v[6:9], v14 offset:1024
	ds_read_b128 v[10:13], v14 offset:2048
	ds_read_b128 v[14:17], v14 offset:3072
	ds_read_b128 v[18:21], v30
	ds_read_b128 v[22:25], v30 offset:1024
	ds_read_b128 v[26:29], v30 offset:2048
	ds_read_b128 v[30:33], v30 offset:3072
	s_add_u32 s68, s68, 0x20000
	s_addc_u32 s69, s69, 0
	s_mov_b32 m0, s73
	v_lshl_add_u64 v[188:189], s[68:69], 0, v[162:163]
	ds_read_b128 v[196:199], v187 offset:32768
	ds_read_b128 v[200:203], v187 offset:33792
	ds_read_b128 v[204:207], v187 offset:34816
	ds_read_b128 v[208:211], v187 offset:35840
	ds_read_b128 v[212:215], v187 offset:36864
	ds_read_b128 v[216:219], v187 offset:37888
	ds_read_b128 v[234:237], v187 offset:38912
	ds_read_b128 v[238:241], v187 offset:39936
	global_load_lds_dwordx4 v[188:189], off
	v_lshl_add_u64 v[188:189], s[68:69], 0, v[164:165]
	s_mov_b32 m0, s75
	s_nop 0
	global_load_lds_dwordx4 v[188:189], off
	s_waitcnt vmcnt(8)
	s_waitcnt lgkmcnt(0)
	s_barrier
	s_setprio 1
	s_waitcnt lgkmcnt(0)
	v_mfma_f32_16x16x128_f8f6f4 v[158:161], v[2:9], v[196:203], v[158:161]
	v_mfma_f32_16x16x128_f8f6f4 v[154:157], v[10:17], v[196:203], v[154:157]
	v_mfma_f32_16x16x128_f8f6f4 v[150:153], v[2:9], v[204:211], v[150:153]
	v_mfma_f32_16x16x128_f8f6f4 v[146:149], v[10:17], v[204:211], v[146:149]
	v_mfma_f32_16x16x128_f8f6f4 v[126:129], v[2:9], v[212:219], v[126:129]
	v_mfma_f32_16x16x128_f8f6f4 v[122:125], v[10:17], v[212:219], v[122:125]
	v_mfma_f32_16x16x128_f8f6f4 v[118:121], v[2:9], v[234:241], v[118:121]
	v_mfma_f32_16x16x128_f8f6f4 v[114:117], v[10:17], v[234:241], v[114:117]
	s_setprio 0
	s_setprio 1
	v_mfma_f32_16x16x128_f8f6f4 v[142:145], v[18:25], v[196:203], v[142:145]
	v_mfma_f32_16x16x128_f8f6f4 v[138:141], v[26:33], v[196:203], v[138:141]
	v_mfma_f32_16x16x128_f8f6f4 v[134:137], v[18:25], v[204:211], v[134:137]
	v_mfma_f32_16x16x128_f8f6f4 v[130:133], v[26:33], v[204:211], v[130:133]
	v_mfma_f32_16x16x128_f8f6f4 v[110:113], v[18:25], v[212:219], v[110:113]
	v_mfma_f32_16x16x128_f8f6f4 v[106:109], v[26:33], v[212:219], v[106:109]
	v_mfma_f32_16x16x128_f8f6f4 v[102:105], v[18:25], v[234:241], v[102:105]
	v_mfma_f32_16x16x128_f8f6f4 v[98:101], v[26:33], v[234:241], v[98:101]
	s_setprio 0
	s_barrier
	s_add_i32 s4, s4, s45
	v_lshl_add_u64 v[174:175], v[174:175], 0, s[22:23]
	s_mov_b32 m0, s4
	ds_read_b128 v[196:199], v187 offset:49152
	ds_read_b128 v[200:203], v187 offset:50176
	ds_read_b128 v[204:207], v187 offset:51200
	ds_read_b128 v[208:211], v187 offset:52224
	ds_read_b128 v[212:215], v187 offset:53248
	ds_read_b128 v[216:219], v187 offset:54272
	ds_read_b128 v[234:237], v187 offset:55296
	ds_read_b128 v[238:241], v187 offset:56320
	global_load_lds_dwordx4 v[174:175], off
	s_add_i32 m0, s4, 0x2000
	s_add_u32 s36, s36, 0x20080
	v_lshl_add_u64 v[174:175], v[176:177], 0, s[22:23]
	s_addc_u32 s37, s37, 0
	s_add_i32 s4, s86, s45
	global_load_lds_dwordx4 v[174:175], off
	v_lshl_add_u64 v[174:175], s[36:37], 0, v[0:1]
	s_mov_b32 m0, s4
	s_nop 0
	global_load_lds_dwordx4 v[174:175], off
	v_lshl_add_u64 v[174:175], s[36:37], 0, v[166:167]
	s_add_i32 m0, s4, 0x2000
	s_nop 0
	global_load_lds_dwordx4 v[174:175], off
	v_lshl_add_u64 v[174:175], v[178:179], 0, s[22:23]
	s_mov_b32 m0, s79
	s_nop 0
	global_load_lds_dwordx4 v[174:175], off
	v_lshl_add_u64 v[174:175], v[180:181], 0, s[22:23]
	s_mov_b32 m0, s82
	s_nop 0
	global_load_lds_dwordx4 v[174:175], off
	s_waitcnt vmcnt(8)
	s_waitcnt lgkmcnt(0)
	s_barrier
	s_setprio 1
	s_waitcnt lgkmcnt(0)
	v_mfma_f32_16x16x128_f8f6f4 v[94:97], v[2:9], v[196:203], v[94:97]
	v_mfma_f32_16x16x128_f8f6f4 v[90:93], v[10:17], v[196:203], v[90:93]
	v_mfma_f32_16x16x128_f8f6f4 v[86:89], v[2:9], v[204:211], v[86:89]
	v_mfma_f32_16x16x128_f8f6f4 v[82:85], v[10:17], v[204:211], v[82:85]
	v_mfma_f32_16x16x128_f8f6f4 v[62:65], v[2:9], v[212:219], v[62:65]
	v_mfma_f32_16x16x128_f8f6f4 v[58:61], v[10:17], v[212:219], v[58:61]
	v_mfma_f32_16x16x128_f8f6f4 v[54:57], v[2:9], v[234:241], v[54:57]
	v_mfma_f32_16x16x128_f8f6f4 v[50:53], v[10:17], v[234:241], v[50:53]
	s_setprio 0
	s_setprio 1
	v_mfma_f32_16x16x128_f8f6f4 v[78:81], v[18:25], v[196:203], v[78:81]
	v_mfma_f32_16x16x128_f8f6f4 v[74:77], v[26:33], v[196:203], v[74:77]
	v_mfma_f32_16x16x128_f8f6f4 v[70:73], v[18:25], v[204:211], v[70:73]
	v_mfma_f32_16x16x128_f8f6f4 v[66:69], v[26:33], v[204:211], v[66:69]
	v_mfma_f32_16x16x128_f8f6f4 v[46:49], v[18:25], v[212:219], v[46:49]
	v_mfma_f32_16x16x128_f8f6f4 v[42:45], v[26:33], v[212:219], v[42:45]
	v_mfma_f32_16x16x128_f8f6f4 v[38:41], v[18:25], v[234:241], v[38:41]
	v_mfma_f32_16x16x128_f8f6f4 v[34:37], v[26:33], v[234:241], v[34:37]
	s_setprio 0
	s_barrier
	s_add_i32 s92, s92, 2
	s_add_u32 s26, s26, 0x100
	s_addc_u32 s27, s27, 0
	s_add_u32 s65, s65, 0x100
	s_addc_u32 s74, s74, 0
	s_cmp_gt_u32 s92, 5
	s_cbranch_scc0 .LBB0_49
	s_ashr_i32 s65, s64, 31
	s_lshl_b32 s26, s66, 8
	s_lshl_b64 s[36:37], s[64:65], 12
	v_or_b32_e32 v2, s26, v185
	s_add_u32 s36, s5, s36
	s_addc_u32 s37, s78, s37
	v_ashrrev_i32_e32 v3, 31, v2
	v_lshl_add_u64 v[6:7], v[2:3], 2, s[36:37]
	global_load_dwordx4 v[10:13], v[6:7], off offset:16
	global_load_dwordx4 v[14:17], v[6:7], off
	global_load_dwordx4 v[2:5], v[6:7], off offset:528
	s_nop 0
	global_load_dwordx4 v[6:9], v[6:7], off offset:512
	s_and_b64 vcc, exec, s[42:43]
	s_cbranch_vccz .LBB0_52
	s_barrier

.LBB0_248:
	v_readlane_b32 s100, v254, 32
	v_and_b32_e32 v250, 3, v194
	v_lshlrev_b32_e32 v250, 5, v250
	v_bfe_u32 v251, v194, 2, 1
	v_lshl_or_b32 v250, v251, 4, v250
	v_bfe_u32 v251, v194, 3, 1
	v_lshl_or_b32 v250, v251, 12, v250
	s_and_b32 s101, s100, 3
	s_lshl_b32 s101, s101, 7
	v_add_u32_e32 v250, s101, v250
	s_lshl_b32 s101, s66, 9
	v_add_u32_e32 v250, s101, v250
	s_lshl_b32 s101, s68, 13
	v_add_u32_e32 v250, s101, v250
	v_mov_b32_e32 v231, s14
	v_add_co_u32_e32 v230, vcc, s5, v250
	s_nop 1
	v_addc_co_u32_e32 v231, vcc, 0, v231, vcc
	s_lshl_b32 s100, s100, 8
	s_add_i32 s100, s100, 0x23400
	v_lshrrev_b32_e32 v233, 4, v194
	v_lshl_add_u32 v233, v233, 4, s100
	s_mov_b32 m0, s100
	s_mov_b64 exec, 0xffff
	global_load_lds_dwordx4 v[230:231], off
	s_mov_b64 exec, -1
	s_ashr_i32 s63, s62, 31
	s_lshl_b64 s[36:37], s[62:63], 21
	s_add_u32 s4, s82, s36
	s_addc_u32 s6, s83, s37
	s_ashr_i32 s61, s60, 31
	s_lshl_b64 s[36:37], s[60:61], 18
	s_add_u32 s64, s4, s36
	s_addc_u32 s65, s6, s37
	s_and_b64 s[36:37], s[70:71], exec
	s_cselect_b32 s6, s65, s27
	s_cselect_b32 s31, s64, s26
	v_mov_b32_e32 v173, v1
	v_mov_b32_e32 v175, v1
	s_add_u32 s61, s26, 0x100
	v_lshl_add_u64 v[176:177], s[54:55], 0, v[174:175]
	v_lshl_add_u64 v[178:179], s[54:55], 0, v[172:173]
	s_addc_u32 s63, s27, 0
	s_mov_b32 s67, -2
	s_mov_b64 s[26:27], 0
	s_add_u32 s4, s46, s26
	s_addc_u32 s36, s47, s27
	s_add_u32 s69, s4, 0x2e000100
	s_addc_u32 s70, s36, 0
	s_add_u32 s74, s61, s26
	s_addc_u32 s86, s63, s27
	s_add_i32 s4, 0, 0x10000
	s_cmpk_eq_i32 s26, 0x300
	s_cselect_b64 vcc, -1, 0
	s_and_b64 s[36:37], vcc, exec
	s_cselect_b32 s71, s41, s70
	s_cselect_b32 s70, s40, s69
	v_add_u32_e32 v0, s4, v200
	s_cselect_b32 s37, s6, s86
	s_cselect_b32 s36, s31, s74
	s_add_i32 s69, 0, 0x14000
	ds_read_b128 v[18:21], v0
	ds_read_b128 v[22:25], v0 offset:1024
	ds_read_b128 v[26:29], v0 offset:2048
	ds_read_b128 v[30:33], v0 offset:3072
	v_add_u32_e32 v0, s69, v200
	ds_read_b128 v[2:5], v0
	ds_read_b128 v[6:9], v0 offset:1024
	ds_read_b128 v[10:13], v0 offset:2048
	ds_read_b128 v[14:17], v0 offset:3072
	v_lshl_add_u64 v[222:223], v[178:179], 0, s[26:27]
	s_add_i32 m0, s93, 0xc000
	ds_read_b128 v[180:183], v201
	ds_read_b128 v[184:187], v201 offset:1024
	ds_read_b128 v[206:209], v201 offset:2048
	ds_read_b128 v[210:213], v201 offset:3072
	ds_read_b128 v[214:217], v201 offset:4096
	ds_read_b128 v[218:221], v201 offset:5120
	ds_read_b128 v[234:237], v201 offset:6144
	ds_read_b128 v[238:241], v201 offset:7168
	global_load_lds_dwordx4 v[222:223], off
	v_lshl_add_u64 v[222:223], v[176:177], 0, s[26:27]
	s_add_i32 m0, s93, 0xe000
	s_nop 0
	global_load_lds_dwordx4 v[222:223], off
	s_waitcnt vmcnt(8)
	s_waitcnt lgkmcnt(0)
	s_barrier
	s_setprio 1
	s_waitcnt lgkmcnt(0)
	v_mfma_f32_16x16x128_f8f6f4 v[158:161], v[18:25], v[180:187], 0
	v_mfma_f32_16x16x128_f8f6f4 v[154:157], v[26:33], v[180:187], 0
	v_mfma_f32_16x16x128_f8f6f4 v[142:145], v[18:25], v[206:213], 0
	v_mfma_f32_16x16x128_f8f6f4 v[138:141], v[26:33], v[206:213], 0
	v_mfma_f32_16x16x128_f8f6f4 v[126:129], v[18:25], v[214:221], 0
	v_mfma_f32_16x16x128_f8f6f4 v[122:125], v[26:33], v[214:221], 0
	v_mfma_f32_16x16x128_f8f6f4 v[110:113], v[18:25], v[234:241], 0
	v_mfma_f32_16x16x128_f8f6f4 v[106:109], v[26:33], v[234:241], 0
	s_setprio 0
	s_setprio 1
	v_mfma_f32_16x16x128_f8f6f4 v[150:153], v[2:9], v[180:187], 0
	v_mfma_f32_16x16x128_f8f6f4 v[146:149], v[10:17], v[180:187], 0
	v_mfma_f32_16x16x128_f8f6f4 v[134:137], v[2:9], v[206:213], 0
	v_mfma_f32_16x16x128_f8f6f4 v[130:133], v[10:17], v[206:213], 0
	v_mfma_f32_16x16x128_f8f6f4 v[118:121], v[2:9], v[214:221], 0
	v_mfma_f32_16x16x128_f8f6f4 v[114:117], v[10:17], v[214:221], 0
	v_mfma_f32_16x16x128_f8f6f4 v[102:105], v[2:9], v[234:241], 0
	v_mfma_f32_16x16x128_f8f6f4 v[98:101], v[10:17], v[234:241], 0
	s_setprio 0
	s_barrier
	s_add_i32 s4, s4, s92
	v_lshl_add_u64 v[180:181], s[36:37], 0, v[162:163]
	s_mov_b32 m0, s4
	ds_read_b128 v[206:209], v201 offset:16384
	ds_read_b128 v[210:213], v201 offset:17408
	ds_read_b128 v[214:217], v201 offset:18432
	ds_read_b128 v[218:221], v201 offset:19456
	ds_read_b128 v[234:237], v201 offset:20480
	ds_read_b128 v[238:241], v201 offset:21504
	ds_read_b128 v[242:245], v201 offset:22528
	ds_read_b128 v[246:249], v201 offset:23552
	global_load_lds_dwordx4 v[180:181], off
	s_add_i32 m0, s4, 0x2000
	s_add_u32 s86, s36, 0x20000
	v_lshl_add_u64 v[182:183], s[36:37], 0, v[164:165]
	s_addc_u32 s87, s37, 0
	s_add_i32 s4, s69, s92
	global_load_lds_dwordx4 v[182:183], off
	v_lshl_add_u64 v[184:185], s[86:87], 0, v[162:163]
	s_mov_b32 m0, s4
	v_cndmask_b32_e32 v0, v168, v202, vcc
	global_load_lds_dwordx4 v[184:185], off
	v_lshl_add_u64 v[184:185], s[86:87], 0, v[164:165]
	s_add_i32 m0, s4, 0x2000
	v_lshl_add_u64 v[186:187], s[70:71], 0, v[0:1]
	global_load_lds_dwordx4 v[184:185], off
	s_mov_b32 m0, s93
	v_cndmask_b32_e32 v184, v170, v203, vcc
	global_load_lds_dwordx4 v0, s[70:71]
	s_mov_b32 m0, s79
	v_mov_b32_e32 v185, v1
	global_load_lds_dwordx4 v184, s[70:71]
	s_waitcnt vmcnt(8)
	s_waitcnt lgkmcnt(0)
	v_lshl_add_u64 v[184:185], s[70:71], 0, v[184:185]
	s_barrier
	s_setprio 1
	s_waitcnt lgkmcnt(0)
	v_mfma_f32_16x16x128_f8f6f4 v[94:97], v[18:25], v[206:213], 0
	v_mfma_f32_16x16x128_f8f6f4 v[90:93], v[26:33], v[206:213], 0
	v_mfma_f32_16x16x128_f8f6f4 v[70:73], v[18:25], v[214:221], 0
	v_mfma_f32_16x16x128_f8f6f4 v[66:69], v[26:33], v[214:221], 0
	v_mfma_f32_16x16x128_f8f6f4 v[54:57], v[18:25], v[234:241], 0
	v_mfma_f32_16x16x128_f8f6f4 v[50:53], v[26:33], v[234:241], 0
	v_mfma_f32_16x16x128_f8f6f4 v[38:41], v[18:25], v[242:249], 0
	v_mfma_f32_16x16x128_f8f6f4 v[34:37], v[26:33], v[242:249], 0
	s_setprio 0
	s_setprio 1
	v_mfma_f32_16x16x128_f8f6f4 v[86:89], v[2:9], v[206:213], 0
	v_mfma_f32_16x16x128_f8f6f4 v[82:85], v[10:17], v[206:213], 0
	v_mfma_f32_16x16x128_f8f6f4 v[78:81], v[2:9], v[214:221], 0
	v_mfma_f32_16x16x128_f8f6f4 v[74:77], v[10:17], v[214:221], 0
	v_mfma_f32_16x16x128_f8f6f4 v[62:65], v[2:9], v[234:241], 0
	v_mfma_f32_16x16x128_f8f6f4 v[58:61], v[10:17], v[234:241], 0
	v_mfma_f32_16x16x128_f8f6f4 v[46:49], v[2:9], v[242:249], 0
	v_mfma_f32_16x16x128_f8f6f4 v[42:45], v[10:17], v[242:249], 0
	s_setprio 0
	s_barrier
	s_add_i32 s4, 0, 0x18000
	v_add_u32_e32 v0, s4, v200
	s_add_i32 s69, 0, 0x1c000
	ds_read_b128 v[2:5], v0
	ds_read_b128 v[6:9], v0 offset:1024
	ds_read_b128 v[10:13], v0 offset:2048
	ds_read_b128 v[14:17], v0 offset:3072
	v_add_u32_e32 v0, s69, v200
	ds_read_b128 v[18:21], v0
	ds_read_b128 v[22:25], v0 offset:1024
	ds_read_b128 v[26:29], v0 offset:2048
	ds_read_b128 v[30:33], v0 offset:3072
	s_mov_b32 m0, s84
	v_cndmask_b32_e32 v0, v172, v204, vcc
	ds_read_b128 v[206:209], v201 offset:32768
	ds_read_b128 v[210:213], v201 offset:33792
	ds_read_b128 v[214:217], v201 offset:34816
	ds_read_b128 v[218:221], v201 offset:35840
	ds_read_b128 v[234:237], v201 offset:36864
	ds_read_b128 v[238:241], v201 offset:37888
	ds_read_b128 v[242:245], v201 offset:38912
	ds_read_b128 v[246:249], v201 offset:39936
	v_cndmask_b32_e32 v173, v174, v205, vcc
	global_load_lds_dwordx4 v0, s[70:71]
	s_mov_b32 m0, s85
	s_nop 0
	global_load_lds_dwordx4 v173, s[70:71]
	s_waitcnt vmcnt(8)
	s_waitcnt lgkmcnt(0)
	s_barrier
	s_setprio 1
	s_waitcnt lgkmcnt(0)
	v_mfma_f32_16x16x128_f8f6f4 v[158:161], v[2:9], v[206:213], v[158:161]
	v_mfma_f32_16x16x128_f8f6f4 v[154:157], v[10:17], v[206:213], v[154:157]
	v_mfma_f32_16x16x128_f8f6f4 v[142:145], v[2:9], v[214:221], v[142:145]
	v_mfma_f32_16x16x128_f8f6f4 v[138:141], v[10:17], v[214:221], v[138:141]
	v_mfma_f32_16x16x128_f8f6f4 v[126:129], v[2:9], v[234:241], v[126:129]
	v_mfma_f32_16x16x128_f8f6f4 v[122:125], v[10:17], v[234:241], v[122:125]
	v_mfma_f32_16x16x128_f8f6f4 v[110:113], v[2:9], v[242:249], v[110:113]
	v_mfma_f32_16x16x128_f8f6f4 v[106:109], v[10:17], v[242:249], v[106:109]
	s_setprio 0
	s_setprio 1
	v_mfma_f32_16x16x128_f8f6f4 v[150:153], v[18:25], v[206:213], v[150:153]
	v_mfma_f32_16x16x128_f8f6f4 v[146:149], v[26:33], v[206:213], v[146:149]
	v_mfma_f32_16x16x128_f8f6f4 v[134:137], v[18:25], v[214:221], v[134:137]
	v_mfma_f32_16x16x128_f8f6f4 v[130:133], v[26:33], v[214:221], v[130:133]
	v_mfma_f32_16x16x128_f8f6f4 v[118:121], v[18:25], v[234:241], v[118:121]
	v_mfma_f32_16x16x128_f8f6f4 v[114:117], v[26:33], v[234:241], v[114:117]
	v_mfma_f32_16x16x128_f8f6f4 v[102:105], v[18:25], v[242:249], v[102:105]
	v_mfma_f32_16x16x128_f8f6f4 v[98:101], v[26:33], v[242:249], v[98:101]
	s_setprio 0
	s_barrier
	s_add_i32 s4, s4, s92
	v_lshl_add_u64 v[180:181], v[180:181], 0, s[22:23]
	s_mov_b32 m0, s4
	ds_read_b128 v[206:209], v201 offset:49152
	ds_read_b128 v[210:213], v201 offset:50176
	ds_read_b128 v[214:217], v201 offset:51200
	ds_read_b128 v[218:221], v201 offset:52224
	ds_read_b128 v[234:237], v201 offset:53248
	ds_read_b128 v[238:241], v201 offset:54272
	ds_read_b128 v[242:245], v201 offset:55296
	ds_read_b128 v[246:249], v201 offset:56320
	global_load_lds_dwordx4 v[180:181], off
	s_add_i32 m0, s4, 0x2000
	s_add_u32 s36, s36, 0x20080
	v_lshl_add_u64 v[180:181], v[182:183], 0, s[22:23]
	s_addc_u32 s37, s37, 0
	s_add_i32 s4, s69, s92
	global_load_lds_dwordx4 v[180:181], off
	v_lshl_add_u64 v[180:181], s[36:37], 0, v[162:163]
	s_mov_b32 m0, s4
	s_nop 0
	global_load_lds_dwordx4 v[180:181], off
	v_lshl_add_u64 v[180:181], s[36:37], 0, v[164:165]
	s_add_i32 m0, s4, 0x2000
	s_nop 0
	global_load_lds_dwordx4 v[180:181], off
	v_lshl_add_u64 v[180:181], v[186:187], 0, s[22:23]
	s_mov_b32 m0, s15
	s_nop 0
	global_load_lds_dwordx4 v[180:181], off
	v_lshl_add_u64 v[180:181], v[184:185], 0, s[22:23]
	s_mov_b32 m0, s16
	s_nop 0
	global_load_lds_dwordx4 v[180:181], off
	s_waitcnt vmcnt(8)
	s_waitcnt lgkmcnt(0)
	s_barrier
	s_setprio 1
	s_waitcnt lgkmcnt(0)
	v_mfma_f32_16x16x128_f8f6f4 v[94:97], v[2:9], v[206:213], v[94:97]
	v_mfma_f32_16x16x128_f8f6f4 v[90:93], v[10:17], v[206:213], v[90:93]
	v_mfma_f32_16x16x128_f8f6f4 v[70:73], v[2:9], v[214:221], v[70:73]
	v_mfma_f32_16x16x128_f8f6f4 v[66:69], v[10:17], v[214:221], v[66:69]
	v_mfma_f32_16x16x128_f8f6f4 v[54:57], v[2:9], v[234:241], v[54:57]
	v_mfma_f32_16x16x128_f8f6f4 v[50:53], v[10:17], v[234:241], v[50:53]
	v_mfma_f32_16x16x128_f8f6f4 v[38:41], v[2:9], v[242:249], v[38:41]
	v_mfma_f32_16x16x128_f8f6f4 v[34:37], v[10:17], v[242:249], v[34:37]
	s_setprio 0
	s_setprio 1
	v_mfma_f32_16x16x128_f8f6f4 v[86:89], v[18:25], v[206:213], v[86:89]
	v_mfma_f32_16x16x128_f8f6f4 v[82:85], v[26:33], v[206:213], v[82:85]
	v_mfma_f32_16x16x128_f8f6f4 v[78:81], v[18:25], v[214:221], v[78:81]
	v_mfma_f32_16x16x128_f8f6f4 v[74:77], v[26:33], v[214:221], v[74:77]
	v_mfma_f32_16x16x128_f8f6f4 v[62:65], v[18:25], v[234:241], v[62:65]
	v_mfma_f32_16x16x128_f8f6f4 v[58:61], v[26:33], v[234:241], v[58:61]
	v_mfma_f32_16x16x128_f8f6f4 v[46:49], v[18:25], v[242:249], v[46:49]
	v_mfma_f32_16x16x128_f8f6f4 v[42:45], v[26:33], v[242:249], v[42:45]
	s_setprio 0
	s_barrier
	s_add_i32 s67, s67, 2
	s_add_u32 s26, s26, 0x100
	s_addc_u32 s27, s27, 0
.LBB0_249:
	s_add_u32 s4, s46, s26
	s_addc_u32 s36, s47, s27
	s_add_u32 s69, s4, 0x2e000100
	s_addc_u32 s70, s36, 0
	s_add_u32 s74, s61, s26
	s_addc_u32 s86, s63, s27
	s_add_i32 s4, 0, 0x10000
	s_cmpk_eq_i32 s26, 0x300
	s_cselect_b64 vcc, -1, 0
	s_and_b64 s[36:37], vcc, exec
	s_cselect_b32 s71, s41, s70
	s_cselect_b32 s70, s40, s69
	v_add_u32_e32 v0, s4, v200
	s_cselect_b32 s37, s6, s86
	s_cselect_b32 s36, s31, s74
	s_add_i32 s69, 0, 0x14000
	ds_read_b128 v[18:21], v0
	ds_read_b128 v[22:25], v0 offset:1024
	ds_read_b128 v[26:29], v0 offset:2048
	ds_read_b128 v[30:33], v0 offset:3072
	v_add_u32_e32 v0, s69, v200
	ds_read_b128 v[2:5], v0
	ds_read_b128 v[6:9], v0 offset:1024
	ds_read_b128 v[10:13], v0 offset:2048
	ds_read_b128 v[14:17], v0 offset:3072
	v_lshl_add_u64 v[222:223], v[178:179], 0, s[26:27]
	s_add_i32 m0, s93, 0xc000
	ds_read_b128 v[180:183], v201
	ds_read_b128 v[184:187], v201 offset:1024
	ds_read_b128 v[206:209], v201 offset:2048
	ds_read_b128 v[210:213], v201 offset:3072
	ds_read_b128 v[214:217], v201 offset:4096
	ds_read_b128 v[218:221], v201 offset:5120
	ds_read_b128 v[234:237], v201 offset:6144
	ds_read_b128 v[238:241], v201 offset:7168
	global_load_lds_dwordx4 v[222:223], off
	v_lshl_add_u64 v[222:223], v[176:177], 0, s[26:27]
	s_add_i32 m0, s93, 0xe000
	s_nop 0
	global_load_lds_dwordx4 v[222:223], off
	s_waitcnt vmcnt(8)
	s_waitcnt lgkmcnt(0)
	s_barrier
	s_setprio 1
	s_waitcnt lgkmcnt(0)
	v_mfma_f32_16x16x128_f8f6f4 v[158:161], v[18:25], v[180:187], v[158:161]
	v_mfma_f32_16x16x128_f8f6f4 v[154:157], v[26:33], v[180:187], v[154:157]
	v_mfma_f32_16x16x128_f8f6f4 v[142:145], v[18:25], v[206:213], v[142:145]
	v_mfma_f32_16x16x128_f8f6f4 v[138:141], v[26:33], v[206:213], v[138:141]
	v_mfma_f32_16x16x128_f8f6f4 v[126:129], v[18:25], v[214:221], v[126:129]
	v_mfma_f32_16x16x128_f8f6f4 v[122:125], v[26:33], v[214:221], v[122:125]
	v_mfma_f32_16x16x128_f8f6f4 v[110:113], v[18:25], v[234:241], v[110:113]
	v_mfma_f32_16x16x128_f8f6f4 v[106:109], v[26:33], v[234:241], v[106:109]
	s_setprio 0
	s_setprio 1
	v_mfma_f32_16x16x128_f8f6f4 v[150:153], v[2:9], v[180:187], v[150:153]
	v_mfma_f32_16x16x128_f8f6f4 v[146:149], v[10:17], v[180:187], v[146:149]
	v_mfma_f32_16x16x128_f8f6f4 v[134:137], v[2:9], v[206:213], v[134:137]
	v_mfma_f32_16x16x128_f8f6f4 v[130:133], v[10:17], v[206:213], v[130:133]
	v_mfma_f32_16x16x128_f8f6f4 v[118:121], v[2:9], v[214:221], v[118:121]
	v_mfma_f32_16x16x128_f8f6f4 v[114:117], v[10:17], v[214:221], v[114:117]
	v_mfma_f32_16x16x128_f8f6f4 v[102:105], v[2:9], v[234:241], v[102:105]
	v_mfma_f32_16x16x128_f8f6f4 v[98:101], v[10:17], v[234:241], v[98:101]
	s_setprio 0
	s_barrier
	s_add_i32 s4, s4, s92
	v_lshl_add_u64 v[180:181], s[36:37], 0, v[162:163]
	s_mov_b32 m0, s4
	ds_read_b128 v[206:209], v201 offset:16384
	ds_read_b128 v[210:213], v201 offset:17408
	ds_read_b128 v[214:217], v201 offset:18432
	ds_read_b128 v[218:221], v201 offset:19456
	ds_read_b128 v[234:237], v201 offset:20480
	ds_read_b128 v[238:241], v201 offset:21504
	ds_read_b128 v[242:245], v201 offset:22528
	ds_read_b128 v[246:249], v201 offset:23552
	global_load_lds_dwordx4 v[180:181], off
	s_add_i32 m0, s4, 0x2000
	s_add_u32 s86, s36, 0x20000
	v_lshl_add_u64 v[182:183], s[36:37], 0, v[164:165]
	s_addc_u32 s87, s37, 0
	s_add_i32 s4, s69, s92
	global_load_lds_dwordx4 v[182:183], off
	v_lshl_add_u64 v[184:185], s[86:87], 0, v[162:163]
	s_mov_b32 m0, s4
	v_cndmask_b32_e32 v0, v168, v202, vcc
	global_load_lds_dwordx4 v[184:185], off
	v_lshl_add_u64 v[184:185], s[86:87], 0, v[164:165]
	s_add_i32 m0, s4, 0x2000
	v_lshl_add_u64 v[186:187], s[70:71], 0, v[0:1]
	global_load_lds_dwordx4 v[184:185], off
	s_mov_b32 m0, s93
	v_cndmask_b32_e32 v184, v170, v203, vcc
	global_load_lds_dwordx4 v0, s[70:71]
	s_mov_b32 m0, s79
	v_mov_b32_e32 v185, v1
	global_load_lds_dwordx4 v184, s[70:71]
	s_waitcnt vmcnt(8)
	s_waitcnt lgkmcnt(0)
	v_lshl_add_u64 v[184:185], s[70:71], 0, v[184:185]
	s_barrier
	s_setprio 1
	s_waitcnt lgkmcnt(0)
	v_mfma_f32_16x16x128_f8f6f4 v[94:97], v[18:25], v[206:213], v[94:97]
	v_mfma_f32_16x16x128_f8f6f4 v[90:93], v[26:33], v[206:213], v[90:93]
	v_mfma_f32_16x16x128_f8f6f4 v[70:73], v[18:25], v[214:221], v[70:73]
	v_mfma_f32_16x16x128_f8f6f4 v[66:69], v[26:33], v[214:221], v[66:69]
	v_mfma_f32_16x16x128_f8f6f4 v[54:57], v[18:25], v[234:241], v[54:57]
	v_mfma_f32_16x16x128_f8f6f4 v[50:53], v[26:33], v[234:241], v[50:53]
	v_mfma_f32_16x16x128_f8f6f4 v[38:41], v[18:25], v[242:249], v[38:41]
	v_mfma_f32_16x16x128_f8f6f4 v[34:37], v[26:33], v[242:249], v[34:37]
	s_setprio 0
	s_setprio 1
	v_mfma_f32_16x16x128_f8f6f4 v[86:89], v[2:9], v[206:213], v[86:89]
	v_mfma_f32_16x16x128_f8f6f4 v[82:85], v[10:17], v[206:213], v[82:85]
	v_mfma_f32_16x16x128_f8f6f4 v[78:81], v[2:9], v[214:221], v[78:81]
	v_mfma_f32_16x16x128_f8f6f4 v[74:77], v[10:17], v[214:221], v[74:77]
	v_mfma_f32_16x16x128_f8f6f4 v[62:65], v[2:9], v[234:241], v[62:65]
	v_mfma_f32_16x16x128_f8f6f4 v[58:61], v[10:17], v[234:241], v[58:61]
	v_mfma_f32_16x16x128_f8f6f4 v[46:49], v[2:9], v[242:249], v[46:49]
	v_mfma_f32_16x16x128_f8f6f4 v[42:45], v[10:17], v[242:249], v[42:45]
	s_setprio 0
	s_barrier
	s_add_i32 s4, 0, 0x18000
	v_add_u32_e32 v0, s4, v200
	s_add_i32 s69, 0, 0x1c000
	ds_read_b128 v[2:5], v0
	ds_read_b128 v[6:9], v0 offset:1024
	ds_read_b128 v[10:13], v0 offset:2048
	ds_read_b128 v[14:17], v0 offset:3072
	v_add_u32_e32 v0, s69, v200
	ds_read_b128 v[18:21], v0
	ds_read_b128 v[22:25], v0 offset:1024
	ds_read_b128 v[26:29], v0 offset:2048
	ds_read_b128 v[30:33], v0 offset:3072
	s_mov_b32 m0, s84
	v_cndmask_b32_e32 v0, v172, v204, vcc
	ds_read_b128 v[206:209], v201 offset:32768
	ds_read_b128 v[210:213], v201 offset:33792
	ds_read_b128 v[214:217], v201 offset:34816
	ds_read_b128 v[218:221], v201 offset:35840
	ds_read_b128 v[234:237], v201 offset:36864
	ds_read_b128 v[238:241], v201 offset:37888
	ds_read_b128 v[242:245], v201 offset:38912
	ds_read_b128 v[246:249], v201 offset:39936
	v_cndmask_b32_e32 v173, v174, v205, vcc
	global_load_lds_dwordx4 v0, s[70:71]
	s_mov_b32 m0, s85
	s_nop 0
	global_load_lds_dwordx4 v173, s[70:71]
	s_waitcnt vmcnt(8)
	s_waitcnt lgkmcnt(0)
	s_barrier
	s_setprio 1
	s_waitcnt lgkmcnt(0)
	v_mfma_f32_16x16x128_f8f6f4 v[158:161], v[2:9], v[206:213], v[158:161]
	v_mfma_f32_16x16x128_f8f6f4 v[154:157], v[10:17], v[206:213], v[154:157]
	v_mfma_f32_16x16x128_f8f6f4 v[142:145], v[2:9], v[214:221], v[142:145]
	v_mfma_f32_16x16x128_f8f6f4 v[138:141], v[10:17], v[214:221], v[138:141]
	v_mfma_f32_16x16x128_f8f6f4 v[126:129], v[2:9], v[234:241], v[126:129]
	v_mfma_f32_16x16x128_f8f6f4 v[122:125], v[10:17], v[234:241], v[122:125]
	v_mfma_f32_16x16x128_f8f6f4 v[110:113], v[2:9], v[242:249], v[110:113]
	v_mfma_f32_16x16x128_f8f6f4 v[106:109], v[10:17], v[242:249], v[106:109]
	s_setprio 0
	s_setprio 1
	v_mfma_f32_16x16x128_f8f6f4 v[150:153], v[18:25], v[206:213], v[150:153]
	v_mfma_f32_16x16x128_f8f6f4 v[146:149], v[26:33], v[206:213], v[146:149]
	v_mfma_f32_16x16x128_f8f6f4 v[134:137], v[18:25], v[214:221], v[134:137]
	v_mfma_f32_16x16x128_f8f6f4 v[130:133], v[26:33], v[214:221], v[130:133]
	v_mfma_f32_16x16x128_f8f6f4 v[118:121], v[18:25], v[234:241], v[118:121]
	v_mfma_f32_16x16x128_f8f6f4 v[114:117], v[26:33], v[234:241], v[114:117]
	v_mfma_f32_16x16x128_f8f6f4 v[102:105], v[18:25], v[242:249], v[102:105]
	v_mfma_f32_16x16x128_f8f6f4 v[98:101], v[26:33], v[242:249], v[98:101]
	s_setprio 0
	s_barrier
	s_add_i32 s4, s4, s92
	v_lshl_add_u64 v[180:181], v[180:181], 0, s[22:23]
	s_mov_b32 m0, s4
	ds_read_b128 v[206:209], v201 offset:49152
	ds_read_b128 v[210:213], v201 offset:50176
	ds_read_b128 v[214:217], v201 offset:51200
	ds_read_b128 v[218:221], v201 offset:52224
	ds_read_b128 v[234:237], v201 offset:53248
	ds_read_b128 v[238:241], v201 offset:54272
	ds_read_b128 v[242:245], v201 offset:55296
	ds_read_b128 v[246:249], v201 offset:56320
	global_load_lds_dwordx4 v[180:181], off
	s_add_i32 m0, s4, 0x2000
	s_add_u32 s36, s36, 0x20080
	v_lshl_add_u64 v[180:181], v[182:183], 0, s[22:23]
	s_addc_u32 s37, s37, 0
	s_add_i32 s4, s69, s92
	global_load_lds_dwordx4 v[180:181], off
	v_lshl_add_u64 v[180:181], s[36:37], 0, v[162:163]
	s_mov_b32 m0, s4
	s_nop 0
	global_load_lds_dwordx4 v[180:181], off
	v_lshl_add_u64 v[180:181], s[36:37], 0, v[164:165]
	s_add_i32 m0, s4, 0x2000
	s_nop 0
	global_load_lds_dwordx4 v[180:181], off
	v_lshl_add_u64 v[180:181], v[186:187], 0, s[22:23]
	s_mov_b32 m0, s15
	s_nop 0
	global_load_lds_dwordx4 v[180:181], off
	v_lshl_add_u64 v[180:181], v[184:185], 0, s[22:23]
	s_mov_b32 m0, s16
	s_nop 0
	global_load_lds_dwordx4 v[180:181], off
	s_waitcnt vmcnt(8)
	s_waitcnt lgkmcnt(0)
	s_barrier
	s_setprio 1
	s_waitcnt lgkmcnt(0)
	v_mfma_f32_16x16x128_f8f6f4 v[94:97], v[2:9], v[206:213], v[94:97]
	v_mfma_f32_16x16x128_f8f6f4 v[90:93], v[10:17], v[206:213], v[90:93]
	v_mfma_f32_16x16x128_f8f6f4 v[70:73], v[2:9], v[214:221], v[70:73]
	v_mfma_f32_16x16x128_f8f6f4 v[66:69], v[10:17], v[214:221], v[66:69]
	v_mfma_f32_16x16x128_f8f6f4 v[54:57], v[2:9], v[234:241], v[54:57]
	v_mfma_f32_16x16x128_f8f6f4 v[50:53], v[10:17], v[234:241], v[50:53]
	v_mfma_f32_16x16x128_f8f6f4 v[38:41], v[2:9], v[242:249], v[38:41]
	v_mfma_f32_16x16x128_f8f6f4 v[34:37], v[10:17], v[242:249], v[34:37]
	s_setprio 0
	s_setprio 1
	v_mfma_f32_16x16x128_f8f6f4 v[86:89], v[18:25], v[206:213], v[86:89]
	v_mfma_f32_16x16x128_f8f6f4 v[82:85], v[26:33], v[206:213], v[82:85]
	v_mfma_f32_16x16x128_f8f6f4 v[78:81], v[18:25], v[214:221], v[78:81]
	v_mfma_f32_16x16x128_f8f6f4 v[74:77], v[26:33], v[214:221], v[74:77]
	v_mfma_f32_16x16x128_f8f6f4 v[62:65], v[18:25], v[234:241], v[62:65]
	v_mfma_f32_16x16x128_f8f6f4 v[58:61], v[26:33], v[234:241], v[58:61]
	v_mfma_f32_16x16x128_f8f6f4 v[46:49], v[18:25], v[242:249], v[46:49]
	v_mfma_f32_16x16x128_f8f6f4 v[42:45], v[26:33], v[242:249], v[42:45]
	s_setprio 0
	s_barrier
	s_add_i32 s67, s67, 2
	s_add_u32 s26, s26, 0x100
	s_addc_u32 s27, s27, 0
	s_cmp_gt_u32 s67, 5
	s_cbranch_scc0 .LBB0_249
	s_ashr_i32 s69, s68, 31
	s_lshl_b32 s66, s66, 7
	s_lshl_b64 s[26:27], s[68:69], 13
	v_or_b32_e32 v2, s66, v169
	s_add_u32 s26, s5, s26
	s_addc_u32 s27, s14, s27
	v_ashrrev_i32_e32 v3, 31, v2
	v_lshl_add_u64 v[6:7], v[2:3], 2, s[26:27]
	s_mov_b64 s[26:27], 0x1000
	v_lshl_add_u64 v[14:15], v[6:7], 0, s[26:27]
	ds_read_b128 v[2:5], v233 offset:64
	ds_read_b128 v[10:13], v233
	v_add_co_u32_e32 v6, vcc, s9, v6
	v_lshl_add_u32 v22, s75, 8, v171
	s_nop 0
	v_addc_co_u32_e32 v7, vcc, 0, v7, vcc
	ds_read_b128 v[6:9], v233 offset:128
	s_nop 0
	ds_read_b128 v[14:17], v233 offset:192
	s_and_b64 vcc, exec, s[58:59]
	s_cbranch_vccz .LBB0_252
	s_barrier
